# attention loop VALU diet: cross-half max exchange moved to rare path, P permlane swaps removed via natural-key V layout, SGPR-base K/V loads, per-lane partial row sums
# speedup vs baseline: 1.0310x; 1.0310x over previous
.LBB0_1426:
	s_mul_i32 s1, s2, 0x480
	s_mul_hi_i32 s0, s2, 0x480
	s_add_u32 s4, s12, s1
	s_addc_u32 s5, s13, s0
	s_mul_i32 s0, s18, 0x60
	s_ashr_i32 s1, s0, 31
	s_lshl_b64 s[0:1], s[0:1], 1
	s_add_u32 s0, s4, s0
	s_addc_u32 s1, s5, s1
	s_add_i32 s3, s3, s18
	s_mul_hi_i32 s5, s3, 0x30c000
	s_mul_i32 s4, s3, 0x30c000
	s_mul_hi_i32 s7, s3, 0x208000
	s_mul_i32 s6, s3, 0x208000
	v_mov_b32_e32 v52, v0
	s_mov_b32 s3, 0x2aaaaaab
	s_add_u32 s8, s14, s4
	v_mul_hi_i32 v2, v52, s3
	v_lshrrev_b32_e32 v3, 31, v2
	v_ashrrev_i32_e32 v2, 1, v2
	v_add_u32_e32 v40, v2, v3
	v_mul_lo_u32 v2, v40, 12
	v_sub_u32_e32 v18, v52, v2
	s_movk_i32 s3, 0x200
	v_mov_b32_e32 v2, 0xff
	v_bitop3_b16 v2, v52, s3, v2 bitop3:0xec
	s_movk_i32 s3, 0x1556
	s_addc_u32 s9, s15, s5
	v_mul_u32_u24_sdwa v10, v2, s3 dst_sel:DWORD dst_unused:UNUSED_PAD src0_sel:WORD_0 src1_sel:DWORD
	v_ashrrev_i32_e32 v14, 3, v52
	s_add_u32 s10, s16, s6
	v_lshrrev_b32_e32 v19, 16, v10
	v_lshlrev_b32_e32 v21, 3, v52
	v_ashrrev_i32_e32 v15, 31, v14
	s_addc_u32 s11, s17, s7
	v_mul_lo_u16_e32 v3, 12, v19
	v_and_b32_e32 v4, 56, v21
	v_lshlrev_b64 v[50:51], 7, v[14:15]
	v_sub_u16_e32 v20, v2, v3
	v_lshl_add_u64 v[2:3], s[10:11], 0, v[50:51]
	v_lshlrev_b32_e32 v82, 1, v4
	v_lshl_add_u64 v[34:35], v[2:3], 0, v[82:83]
	v_lshlrev_b32_e32 v36, 3, v18
	v_mov_b64_e32 v[2:3], s[8:9]
	s_movk_i32 s3, 0xc0
	v_ashrrev_i32_e32 v37, 31, v36
	v_mad_i64_i32 v[2:3], s[10:11], v40, s3, v[2:3]
	v_alignbit_b32 v10, v20, v10, 16
	s_mov_b32 s3, 0x80060
	v_lshl_add_u64 v[6:7], v[36:37], 1, v[2:3]
	v_pk_mul_lo_u16 v53, v10, s3
	global_load_dwordx4 v[2:5], v[34:35], off
	s_nop 0
	global_load_dwordx4 v[6:9], v[6:7], off
	v_add_u16_sdwa v10, v53, v53 dst_sel:DWORD dst_unused:UNUSED_PAD src0_sel:DWORD src1_sel:WORD_1
	v_lshlrev_b32_e32 v38, 1, v10
	global_load_dwordx4 v[10:13], v38, s[8:9]
	v_ashrrev_i32_e32 v39, 1, v52
	s_movk_i32 s3, 0xffe0
	v_bfe_u32 v155, v52, 5, 1
	v_bfi_b32 v15, s3, v39, v52
	v_mov_b64_e32 v[16:17], s[0:1]
	s_movk_i32 s0, 0x480
	v_mad_i64_i32 v[16:17], s[0:1], v15, s0, v[16:17]
	v_lshlrev_b32_e32 v138, 4, v155
	v_mov_b32_e32 v139, v83
	v_lshl_add_u64 v[16:17], v[16:17], 0, v[138:139]
	global_load_dwordx4 v[106:109], v[16:17], off
	global_load_dwordx4 v[102:105], v[16:17], off offset:32
	global_load_dwordx4 v[98:101], v[16:17], off offset:64
	global_load_dwordx4 v[94:97], v[16:17], off offset:96
	global_load_dwordx4 v[90:93], v[16:17], off offset:128
	global_load_dwordx4 v[86:89], v[16:17], off offset:160
	v_and_b32_e32 v22, 0x1fffff0, v14
	v_lshlrev_b32_e32 v23, 0, v14
	v_lshlrev_b32_e32 v15, 4, v52
	v_lshrrev_b32_e32 v24, 0, v14
	v_and_b32_e32 v14, 3, v14
	v_and_or_b32 v22, v23, 8, v22
	v_bfe_u32 v21, v21, 5, 1
	v_and_b32_e32 v25, 48, v15
	v_and_or_b32 v14, v24, 4, v14
	v_lshrrev_b32_e32 v22, 2, v22
	v_and_b32_e32 v139, 31, v52
	v_lshl_or_b32 v14, v14, 6, v25
	v_or_b32_e32 v21, v22, v21
	v_lshlrev_b32_e32 v23, 8, v40
	v_lshlrev_b32_e32 v24, 8, v19
	v_bitop3_b32 v18, v40, v18, 15 bitop3:0x6c
	v_lshl_or_b32 v14, v21, 9, v14
	v_bitop3_b32 v19, v19, v20, 15 bitop3:0x6c
	v_lshlrev_b32_e32 v41, 8, v139
	v_and_b32_e32 v56, 0xf0, v15
	v_lshl_add_u32 v163, v18, 4, v23
	v_lshl_or_b32 v164, v19, 4, v24
	v_add_u32_e32 v165, 0, v14
	v_bitop3_b32 v167, v138, v41, v56 bitop3:0xde
	v_add_u32_e32 v54, 0, v163
	v_add_u32_e32 v55, 0, v164
	s_waitcnt vmcnt(0)
	v_or_b32_e32 v42, 32, v138
	v_bitop3_b32 v168, v42, v41, v56 bitop3:0xde
	v_add_u32_e32 v46, 0, v168
	s_waitcnt vmcnt(8)
	ds_write_b128 v165, v[2:5]
	s_waitcnt vmcnt(7)
	ds_write_b128 v54, v[6:9] offset:24576
	s_waitcnt vmcnt(6)
	ds_write_b128 v55, v[10:13] offset:24576
	v_add_u32_e32 v6, 0, v167
	s_waitcnt lgkmcnt(0)
	s_barrier
	ds_read_b128 v[2:5], v6 offset:24576
	ds_read_b128 v[6:9], v6 offset:32768
	s_waitcnt vmcnt(5) lgkmcnt(1)
	v_mfma_f32_32x32x16_bf16 v[18:33], v[2:5], v[106:109], 0
	ds_read_b128 v[42:45], v46 offset:24576
	ds_read_b128 v[46:49], v46 offset:32768
	v_mov_b32_e32 v84, v83
	v_mov_b32_e32 v85, v83
	v_readlane_b32 s20, v252, 22
	v_readlane_b32 s22, v252, 24
	v_readlane_b32 s23, v252, 25
	v_readlane_b32 s21, v252, 23
	s_waitcnt lgkmcnt(2)
	v_mfma_f32_32x32x16_bf16 v[2:17], v[6:9], v[106:109], 0
	v_mov_b32_e32 v110, v83
	v_mov_b32_e32 v111, v83
	v_mov_b32_e32 v112, v83
	v_mov_b32_e32 v113, v83
	s_waitcnt vmcnt(4) lgkmcnt(1)
	v_mfma_f32_32x32x16_bf16 v[18:33], v[42:45], v[102:105], v[18:33]
	v_or_b32_e32 v42, 64, v138
	v_bitop3_b32 v166, v42, v41, v56 bitop3:0xde
	s_waitcnt lgkmcnt(0)
	v_mfma_f32_32x32x16_bf16 v[2:17], v[46:49], v[102:105], v[2:17]
	v_add_u32_e32 v46, 0, v166
	ds_read_b128 v[42:45], v46 offset:24576
	ds_read_b128 v[46:49], v46 offset:32768
	s_waitcnt vmcnt(3) lgkmcnt(1)
	v_mfma_f32_32x32x16_bf16 v[18:33], v[42:45], v[98:101], v[18:33]
	v_or_b32_e32 v42, 0x60, v138
	v_bitop3_b32 v162, v42, v41, v56 bitop3:0xde
	s_waitcnt lgkmcnt(0)
	v_mfma_f32_32x32x16_bf16 v[2:17], v[46:49], v[98:101], v[2:17]
	v_add_u32_e32 v46, 0, v162
	ds_read_b128 v[42:45], v46 offset:24576
	ds_read_b128 v[46:49], v46 offset:32768
	s_waitcnt vmcnt(2) lgkmcnt(1)
	v_mfma_f32_32x32x16_bf16 v[18:33], v[42:45], v[94:97], v[18:33]
	v_or_b32_e32 v42, 0x80, v138
	v_bitop3_b32 v161, v42, v41, v56 bitop3:0xde
	s_waitcnt lgkmcnt(0)
	v_mfma_f32_32x32x16_bf16 v[2:17], v[46:49], v[94:97], v[2:17]
	v_add_u32_e32 v46, 0, v161
	ds_read_b128 v[42:45], v46 offset:24576
	ds_read_b128 v[46:49], v46 offset:32768
	s_waitcnt vmcnt(1) lgkmcnt(1)
	v_mfma_f32_32x32x16_bf16 v[18:33], v[42:45], v[90:93], v[18:33]
	v_or_b32_e32 v42, 0xa0, v138
	v_bitop3_b32 v160, v42, v41, v56 bitop3:0xde
	v_add_u32_e32 v41, 0, v160
	s_waitcnt lgkmcnt(0)
	v_mfma_f32_32x32x16_bf16 v[2:17], v[46:49], v[90:93], v[2:17]
	ds_read_b128 v[42:45], v41 offset:24576
	ds_read_b128 v[46:49], v41 offset:32768
	v_and_b32_e32 v41, 63, v52
	v_cmp_gt_u32_e64 s[0:1], 32, v41
	s_waitcnt vmcnt(0) lgkmcnt(1)
	v_mfma_f32_32x32x16_bf16 v[18:33], v[42:45], v[86:89], v[18:33]
	v_mov_b32_e32 v42, 0x3f80
	v_cndmask_b32_e64 v82, 0, v42, s[0:1]
	v_mov_b64_e32 v[44:45], s[22:23]
	v_mov_b64_e32 v[42:43], s[20:21]
	s_waitcnt lgkmcnt(0)
	v_mfma_f32_32x32x16_bf16 v[2:17], v[46:49], v[86:89], v[2:17]
	v_mfma_f32_32x32x16_bf16 v[18:33], v[82:85], v[42:45], v[18:33]
	v_mfma_f32_32x32x16_bf16 v[2:17], v[82:85], v[42:45], v[2:17]
	s_nop 10
	v_max_f32_e32 v42, v19, v19
	v_max_f32_e32 v43, v18, v18
	v_max_f32_e32 v42, v43, v42
	v_max3_f32 v42, v42, v20, v21
	v_max3_f32 v42, v42, v22, v23
	v_max3_f32 v42, v42, v24, v25
	v_max3_f32 v42, v42, v26, v27
	v_max3_f32 v42, v42, v28, v29
	v_max3_f32 v42, v42, v30, v31
	v_max3_f32 v42, v42, v32, v33
	v_max3_f32 v42, v42, v2, v3
	v_max3_f32 v42, v42, v4, v5
	v_max3_f32 v42, v42, v6, v7
	v_max3_f32 v42, v42, v8, v9
	v_max3_f32 v42, v42, v10, v11
	v_max3_f32 v42, v42, v12, v13
	v_max3_f32 v42, v42, v14, v15
	v_max3_f32 v42, v42, v16, v17
	v_mov_b32_e32 v43, v42
	s_nop 1
	v_permlane32_swap_b32_e32 v42, v43
	v_max_f32_e32 v43, v43, v43
	v_max_f32_e32 v42, v42, v42
	v_max_f32_e32 v42, v42, v43
	v_cvt_pk_bf16_f32 v42, v42, v83
	s_nop 0
	v_lshlrev_b32_e32 v159, 16, v42
	s_and_saveexec_b64 s[10:11], s[0:1]
	s_cbranch_execz .LBB0_1428
	v_xor_b32_e32 v42, 0x80000000, v159
	v_cvt_pk_bf16_f32 v42, v42, v83
	v_mov_b32_e32 v111, v83
	v_and_b32_e32 v110, 0xffff, v42
	v_mov_b32_e32 v112, v83
	v_mov_b32_e32 v113, v83
.LBB0_1428:
	s_or_b64 exec, exec, s[10:11]
	v_and_b32_e32 v140, 0xffffffe0, v39
	s_movk_i32 s20, 0xc0
	v_mov_b32_e32 v39, v83
	v_add_u32_e32 v44, 64, v40
	v_mov_b64_e32 v[42:43], s[8:9]
	v_lshl_add_u64 v[38:39], s[8:9], 0, v[38:39]
	v_sub_f32_e32 v46, v18, v159
	v_add_co_u32_e32 v18, vcc, s66, v34
	v_mad_i64_i32 v[44:45], s[8:9], v44, s20, v[42:43]
	v_sub_f32_e32 v47, v19, v159
	v_addc_co_u32_e32 v19, vcc, 0, v35, vcc
	v_lshlrev_b64 v[70:71], 1, v[36:37]
	s_movk_i32 s8, 0x3000
	v_lshl_add_u64 v[36:37], v[44:45], 0, v[70:71]
	global_load_dwordx4 v[56:59], v[18:19], off
	global_load_dwordx4 v[60:63], v[36:37], off
	v_add_co_u32_e32 v18, vcc, s8, v38
	s_movk_i32 s8, 0x6000
	s_nop 0
	v_addc_co_u32_e32 v19, vcc, 0, v39, vcc
	global_load_dwordx4 v[64:67], v[18:19], off
	v_sub_f32_e32 v18, v20, v159
	v_sub_f32_e32 v19, v21, v159
	v_exp_f32_e32 v227, v18
	v_add_co_u32_e32 v18, vcc, s8, v38
	v_exp_f32_e32 v230, v19
	s_nop 0
	v_addc_co_u32_e32 v19, vcc, 0, v39, vcc
	global_load_dwordx4 v[122:125], v[18:19], off
	v_add_u32_e32 v18, 0x80, v40
	v_sub_f32_e32 v20, v22, v159
	v_mad_i64_i32 v[18:19], s[8:9], v18, s20, v[42:43]
	v_sub_f32_e32 v21, v23, v159
	v_exp_f32_e32 v231, v20
	v_lshl_add_u64 v[18:19], v[18:19], 0, v[70:71]
	v_add_co_u32_e32 v20, vcc, s69, v34
	v_exp_f32_e32 v232, v21
	s_nop 0
	v_addc_co_u32_e32 v21, vcc, 0, v35, vcc
	global_load_dwordx4 v[118:121], v[18:19], off
	global_load_dwordx4 v[114:117], v[20:21], off
	v_mad_i64_i32 v[68:69], s[10:11], v40, s20, 0
	s_movk_i32 s11, 0x200
	v_sub_f32_e32 v34, v2, v159
	v_or_b32_sdwa v2, v52, s11 dst_sel:DWORD dst_unused:UNUSED_PAD src0_sel:BYTE_0 src1_sel:DWORD
	s_mov_b32 s11, 0x15555556
	v_sub_f32_e32 v36, v4, v159
	v_sub_f32_e32 v35, v3, v159
	v_mul_hi_u32 v4, v2, s11
	v_mov_b64_e32 v[2:3], s[4:5]
	s_mov_b32 s11, 0xffff
	v_and_b32_e32 v18, 0x3fffffc0, v52
	v_readlane_b32 s8, v252, 28
	v_lshlrev_b32_e32 v19, 4, v41
	v_mad_u64_u32 v[2:3], s[20:21], v4, s20, v[2:3]
	v_and_b32_sdwa v4, s11, v53 dst_sel:DWORD dst_unused:UNUSED_PAD src0_sel:DWORD src1_sel:WORD_1
	v_sub_f32_e32 v22, v24, v159
	v_sub_f32_e32 v23, v25, v159
	v_sub_f32_e32 v24, v26, v159
	v_sub_f32_e32 v25, v27, v159
	v_sub_f32_e32 v26, v28, v159
	v_sub_f32_e32 v27, v29, v159
	v_sub_f32_e32 v28, v30, v159
	v_sub_f32_e32 v29, v31, v159
	v_sub_f32_e32 v30, v32, v159
	v_sub_f32_e32 v31, v33, v159
	v_lshl_add_u32 v141, v18, 2, s8
	v_lshlrev_b32_e32 v18, 3, v41
	v_and_b32_e32 v19, 0xc0, v19
	v_lshlrev_b32_e32 v20, 1, v41
	v_sub_f32_e32 v37, v5, v159
	v_lshlrev_b32_e32 v4, 1, v4
	v_mov_b32_e32 v5, v83
	v_exp_f32_e32 v222, v46
	v_exp_f32_e32 v223, v47
	v_exp_f32_e32 v233, v22
	v_exp_f32_e32 v234, v23
	v_exp_f32_e32 v235, v24
	v_exp_f32_e32 v236, v25
	v_exp_f32_e32 v237, v26
	v_exp_f32_e32 v238, v27
	v_exp_f32_e32 v239, v28
	v_exp_f32_e32 v240, v29
	v_exp_f32_e32 v241, v30
	v_exp_f32_e32 v246, v31
	v_and_or_b32 v19, v18, 24, v19
	v_and_b32_e32 v20, 32, v20
	v_and_b32_e32 v18, 0x100, v18
	v_lshl_add_u64 v[142:143], v[2:3], 0, v[4:5]
	v_lshl_add_u64 v[2:3], s[4:5], 0, v[68:69]
	v_and_b32_e32 v4, 7, v52
	v_or3_b32 v18, v19, v20, v18
	v_sub_f32_e32 v49, v17, v159
	v_sub_f32_e32 v48, v16, v159
	s_waitcnt vmcnt(3)
	v_lshl_add_u64 v[144:145], v[2:3], 0, v[70:71]
	v_lshl_add_u64 v[2:3], s[6:7], 0, v[50:51]
	v_lshlrev_b32_e32 v4, 4, v4
	v_mov_b32_e32 v16, v83
	v_mov_b32_e32 v17, v83
	v_add_u32_e32 v158, 0, v18
	v_sub_f32_e32 v47, v15, v159
	v_sub_f32_e32 v46, v14, v159
	v_sub_f32_e32 v45, v13, v159
	v_sub_f32_e32 v44, v12, v159
	v_sub_f32_e32 v43, v11, v159
	v_sub_f32_e32 v42, v10, v159
	v_sub_f32_e32 v41, v9, v159
	v_sub_f32_e32 v40, v8, v159
	v_sub_f32_e32 v39, v7, v159
	v_sub_f32_e32 v38, v6, v159
	v_lshl_add_u64 v[146:147], v[2:3], 0, v[4:5]
	v_mov_b32_e32 v2, v83
	v_mov_b32_e32 v3, v83
	v_mov_b32_e32 v4, v83
	v_mov_b32_e32 v6, v83
	v_mov_b32_e32 v7, v83
	v_mov_b32_e32 v8, v83
	v_mov_b32_e32 v9, v83
	v_mov_b32_e32 v10, v83
	v_mov_b32_e32 v11, v83
	v_mov_b32_e32 v12, v83
	v_mov_b32_e32 v13, v83
	v_mov_b32_e32 v14, v83
	v_mov_b32_e32 v15, v83
	v_mov_b64_e32 v[32:33], v[16:17]
	s_ashr_i32 s3, s2, 31
	s_mov_b32 s22, 2
	s_mov_b32 s8, 4
	s_mov_b32 s10, 1
	s_mov_b32 s9, 0
	v_lshl_add_u32 v156, v139, 2, v141
	v_mov_b32_e32 v157, 0
	v_mov_b32_e32 v169, 1.0
	v_mov_b64_e32 v[30:31], v[14:15]
	v_mov_b64_e32 v[28:29], v[12:13]
	v_mov_b64_e32 v[26:27], v[10:11]
	v_mov_b64_e32 v[24:25], v[8:9]
	v_mov_b64_e32 v[22:23], v[6:7]
	v_mov_b64_e32 v[20:21], v[4:5]
	v_mov_b64_e32 v[18:19], v[2:3]
	s_waitcnt vmcnt(5)
	ds_write_b128 v165, v[56:59] offset:8192
	s_waitcnt vmcnt(4)
	ds_write_b128 v54, v[60:63] offset:40960
	s_waitcnt vmcnt(3)
	ds_write_b128 v55, v[64:67] offset:40960
	s_waitcnt lgkmcnt(0)
	s_barrier
	v_subrev_u32_e32 v142, s4, v142
	v_subrev_u32_e32 v144, s4, v144
	v_subrev_u32_e32 v146, s6, v146
	s_add_u32 s82, s14, s4
	s_addc_u32 s83, s15, s5
	s_add_u32 s82, s82, 0x9000
	s_addc_u32 s83, s83, 0
	s_add_u32 s84, s16, s6
	s_addc_u32 s85, s17, s7
	s_add_u32 s84, s84, 0x6000
	s_addc_u32 s85, s85, 0
.LBB0_1429:
	s_mov_b32 s4, s9
	s_mov_b32 s9, s22
	s_lshl_b32 s5, s10, 14
	s_add_i32 s5, s5, 0
	v_add_u32_e32 v54, s5, v167
	ds_read_b128 v[50:53], v54 offset:24576
	ds_read_b128 v[54:57], v54 offset:32768
	v_add_u32_e32 v148, s5, v168
	ds_read_b128 v[170:173], v148 offset:24576
	ds_read_b128 v[174:177], v148 offset:32768
	v_add_u32_e32 v148, s5, v166
	s_waitcnt lgkmcnt(3)
	v_mfma_f32_32x32x16_bf16 v[66:81], v[50:53], v[106:109], 0
	v_exp_f32_e32 v153, v35
	v_exp_f32_e32 v178, v42
	v_exp_f32_e32 v179, v43
	v_exp_f32_e32 v180, v44
	v_exp_f32_e32 v181, v45
	v_exp_f32_e32 v182, v46
	v_exp_f32_e32 v183, v47
	s_waitcnt lgkmcnt(2)
	v_mfma_f32_32x32x16_bf16 v[50:65], v[54:57], v[106:109], 0
	v_exp_f32_e32 v184, v48
	v_exp_f32_e32 v49, v49
	s_waitcnt lgkmcnt(1)
	v_mfma_f32_32x32x16_bf16 v[66:81], v[170:173], v[102:105], v[66:81]
	s_waitcnt lgkmcnt(0)
	v_mfma_f32_32x32x16_bf16 v[50:65], v[174:177], v[102:105], v[50:65]
	ds_read_b128 v[170:173], v148 offset:24576
	ds_read_b128 v[174:177], v148 offset:32768
	v_add_u32_e32 v148, s5, v162
	s_waitcnt lgkmcnt(1)
	v_mfma_f32_32x32x16_bf16 v[66:81], v[170:173], v[98:101], v[66:81]
	s_waitcnt lgkmcnt(0)
	v_mfma_f32_32x32x16_bf16 v[50:65], v[174:177], v[98:101], v[50:65]
	ds_read_b128 v[170:173], v148 offset:24576
	ds_read_b128 v[174:177], v148 offset:32768
	v_add_u32_e32 v148, s5, v161
	s_waitcnt lgkmcnt(1)
	v_mfma_f32_32x32x16_bf16 v[66:81], v[170:173], v[94:97], v[66:81]
	s_waitcnt lgkmcnt(0)
	v_mfma_f32_32x32x16_bf16 v[50:65], v[174:177], v[94:97], v[50:65]
	ds_read_b128 v[170:173], v148 offset:24576
	ds_read_b128 v[174:177], v148 offset:32768
	v_add_u32_e32 v148, s5, v160
	s_waitcnt lgkmcnt(1)
	v_mfma_f32_32x32x16_bf16 v[66:81], v[170:173], v[90:93], v[66:81]
	s_waitcnt lgkmcnt(0)
	v_mfma_f32_32x32x16_bf16 v[50:65], v[174:177], v[90:93], v[50:65]
	ds_read_b128 v[170:173], v148 offset:24576
	ds_read_b128 v[174:177], v148 offset:32768
	v_exp_f32_e32 v148, v34
	v_add_f32_e32 v34, 0, v222
	v_add_f32_e32 v34, v223, v34
	v_add_f32_e32 v34, v227, v34
	v_add_f32_e32 v34, v230, v34
	v_add_f32_e32 v34, v231, v34
	v_add_f32_e32 v34, v232, v34
	v_add_f32_e32 v34, v233, v34
	v_add_f32_e32 v34, v234, v34
	v_add_f32_e32 v34, v235, v34
	v_add_f32_e32 v34, v236, v34
	v_add_f32_e32 v34, v237, v34
	v_add_f32_e32 v34, v238, v34
	v_add_f32_e32 v34, v239, v34
	v_add_f32_e32 v34, v240, v34
	s_waitcnt lgkmcnt(1)
	v_mfma_f32_32x32x16_bf16 v[66:81], v[170:173], v[86:89], v[66:81]
	v_exp_f32_e32 v172, v36
	v_add_f32_e32 v34, v241, v34
	v_exp_f32_e32 v173, v37
	v_add_f32_e32 v34, v246, v34
	v_add_f32_e32 v34, v148, v34
	v_add_f32_e32 v34, v153, v34
	v_add_f32_e32 v34, v172, v34
	s_waitcnt lgkmcnt(0)
	v_mfma_f32_32x32x16_bf16 v[50:65], v[174:177], v[86:89], v[50:65]
	v_lshl_add_u32 v247, s4, 13, v158
	ds_read_b64_tr_b16 v[206:207], v247 offset:0
	ds_read_b64_tr_b16 v[208:209], v247 offset:0x400
	ds_read_b64_tr_b16 v[210:211], v247 offset:0x800
	ds_read_b64_tr_b16 v[212:213], v247 offset:0xc00
	ds_read_b64_tr_b16 v[214:215], v247 offset:0x1000
	ds_read_b64_tr_b16 v[216:217], v247 offset:0x1400
	ds_read_b64_tr_b16 v[218:219], v247 offset:0x1800
	ds_read_b64_tr_b16 v[220:221], v247 offset:0x1c00
	v_exp_f32_e32 v174, v38
	v_exp_f32_e32 v175, v39
	v_exp_f32_e32 v176, v40
	v_exp_f32_e32 v177, v41
	v_add_f32_e32 v34, v173, v34
	v_add_f32_e32 v34, v174, v34
	v_add_f32_e32 v34, v175, v34
	v_add_f32_e32 v34, v176, v34
	v_add_f32_e32 v34, v177, v34
	v_add_f32_e32 v34, v178, v34
	v_add_f32_e32 v34, v179, v34
	v_mfma_f32_32x32x16_bf16 v[66:81], v[82:85], v[110:113], v[66:81]
	v_add_f32_e32 v34, v180, v34
	v_add_f32_e32 v34, v181, v34
	v_add_f32_e32 v34, v182, v34
	v_add_f32_e32 v34, v183, v34
	v_add_f32_e32 v34, v184, v34
	v_add_f32_e32 v170, v49, v34
	v_mfma_f32_32x32x16_bf16 v[50:65], v[82:85], v[110:113], v[50:65]
	v_cvt_pk_bf16_f32 v34, v222, v223
	v_cvt_pk_bf16_f32 v35, v227, v230
	v_cvt_pk_bf16_f32 v36, v231, v232
	v_cvt_pk_bf16_f32 v37, v233, v234
	v_cvt_pk_bf16_f32 v38, v235, v236
	v_cvt_pk_bf16_f32 v39, v237, v238
	v_cvt_pk_bf16_f32 v40, v239, v240
	v_cvt_pk_bf16_f32 v41, v241, v246
	v_cvt_pk_bf16_f32 v42, v148, v153
	v_cvt_pk_bf16_f32 v43, v172, v173
	v_cvt_pk_bf16_f32 v44, v174, v175
	v_cvt_pk_bf16_f32 v45, v176, v177
	v_cvt_pk_bf16_f32 v46, v178, v179
	v_cvt_pk_bf16_f32 v47, v180, v181
	v_cvt_pk_bf16_f32 v48, v182, v183
	v_cvt_pk_bf16_f32 v49, v184, v49
	global_load_dwordx4 v[130:133], v146, s[84:85]
	global_load_dwordx4 v[126:129], v144, s[82:83]
	global_load_dwordx4 v[134:137], v142, s[82:83]
	s_add_u32 s82, s82, 0x3000
	s_addc_u32 s83, s83, 0
	s_add_u32 s84, s84, 0x2000
	s_addc_u32 s85, s85, 0
	s_waitcnt lgkmcnt(0)
	s_nop 0
	v_mfma_f32_32x32x16_bf16 v[2:17], v[34:37], v[206:209], v[2:17]
	ds_read_b64_tr_b16 v[172:173], v247 offset:0x200
	ds_read_b64_tr_b16 v[174:175], v247 offset:0x600
	v_max_f32_e32 v249, v67, v67
	v_max_f32_e32 v248, v66, v66
	v_max_f32_e32 v248, v248, v249
	v_max3_f32 v248, v248, v68, v69
	v_max3_f32 v248, v248, v70, v71
	v_mfma_f32_32x32x16_bf16 v[2:17], v[38:41], v[210:213], v[2:17]
	ds_read_b64_tr_b16 v[176:177], v247 offset:0xa00
	ds_read_b64_tr_b16 v[178:179], v247 offset:0xe00
	v_max3_f32 v248, v248, v72, v73
	v_max3_f32 v248, v248, v74, v75
	v_max3_f32 v248, v248, v76, v77
	v_max3_f32 v248, v248, v78, v79
	v_mfma_f32_32x32x16_bf16 v[2:17], v[42:45], v[214:217], v[2:17]
	ds_read_b64_tr_b16 v[180:181], v247 offset:0x1200
	ds_read_b64_tr_b16 v[182:183], v247 offset:0x1600
	v_max3_f32 v248, v248, v80, v81
	v_max3_f32 v248, v248, v50, v51
	v_max3_f32 v248, v248, v52, v53
	v_max3_f32 v248, v248, v54, v55
	v_mfma_f32_32x32x16_bf16 v[2:17], v[46:49], v[218:221], v[2:17]
	ds_read_b64_tr_b16 v[184:185], v247 offset:0x1a00
	ds_read_b64_tr_b16 v[186:187], v247 offset:0x1e00
	v_max3_f32 v248, v248, v56, v57
	v_max3_f32 v248, v248, v58, v59
	v_max3_f32 v248, v248, v60, v61
	v_max3_f32 v248, v248, v62, v63
	v_max3_f32 v248, v248, v64, v65
	s_lshl_b32 s11, s9, 13
	s_lshl_b32 s4, s9, 14
	s_add_i32 s6, s4, 0
	s_waitcnt vmcnt(3)
	v_add_u32_e32 v247, s11, v165
	ds_write_b128 v247, v[114:117]
	v_add_u32_e32 v247, s6, v163
	ds_write_b128 v247, v[118:121] offset:24576
	v_add_u32_e32 v247, s6, v164
	ds_write_b128 v247, v[122:125] offset:24576
	s_waitcnt lgkmcnt(3)
	v_mfma_f32_32x32x16_bf16 v[18:33], v[34:37], v[172:175], v[18:33]
	v_exp_f32_e32 v222, v66
	v_exp_f32_e32 v223, v67
	v_exp_f32_e32 v227, v68
	v_exp_f32_e32 v230, v69
	v_mfma_f32_32x32x16_bf16 v[18:33], v[38:41], v[176:179], v[18:33]
	v_exp_f32_e32 v231, v70
	v_exp_f32_e32 v232, v71
	v_exp_f32_e32 v233, v72
	v_exp_f32_e32 v234, v73
	v_mfma_f32_32x32x16_bf16 v[18:33], v[42:45], v[180:183], v[18:33]
	v_exp_f32_e32 v235, v74
	v_exp_f32_e32 v236, v75
	v_exp_f32_e32 v237, v76
	v_exp_f32_e32 v238, v77
	v_mfma_f32_32x32x16_bf16 v[18:33], v[46:49], v[184:187], v[18:33]
	v_exp_f32_e32 v239, v78
	v_exp_f32_e32 v240, v79
	v_exp_f32_e32 v241, v80
	v_exp_f32_e32 v246, v81
	s_mov_b32 s4, 0x41380000
	v_cmp_ge_f32_e32 vcc, s4, v248
	s_cmp_eq_u64 vcc, exec
	s_cbranch_scc0 .LBB0_1448
	v_mov_b32_e32 v172, 1.0
.LBB0_1437:
	s_waitcnt lgkmcnt(0)
	s_barrier
	v_add_u32_e32 v38, s6, v167
	ds_read_b128 v[34:37], v38 offset:24576
	ds_read_b128 v[38:41], v38 offset:32768
	v_add_u32_e32 v173, s6, v168
	ds_read_b128 v[174:177], v173 offset:24576
	ds_read_b128 v[178:181], v173 offset:32768
	v_add_u32_e32 v173, s6, v166
	s_waitcnt lgkmcnt(3)
	v_mfma_f32_32x32x16_bf16 v[66:81], v[34:37], v[106:109], 0
	v_exp_f32_e32 v198, v57
	v_exp_f32_e32 v199, v58
	v_exp_f32_e32 v200, v59
	v_exp_f32_e32 v201, v60
	v_exp_f32_e32 v202, v61
	v_exp_f32_e32 v203, v62
	v_exp_f32_e32 v204, v63
	s_waitcnt lgkmcnt(2)
	v_mfma_f32_32x32x16_bf16 v[34:49], v[38:41], v[106:109], 0
	v_exp_f32_e32 v205, v64
	v_exp_f32_e32 v65, v65
	s_waitcnt lgkmcnt(1)
	v_mfma_f32_32x32x16_bf16 v[66:81], v[174:177], v[102:105], v[66:81]
	s_waitcnt lgkmcnt(0)
	v_mfma_f32_32x32x16_bf16 v[34:49], v[178:181], v[102:105], v[34:49]
	ds_read_b128 v[174:177], v173 offset:24576
	ds_read_b128 v[178:181], v173 offset:32768
	v_add_u32_e32 v173, s6, v162
	s_waitcnt lgkmcnt(1)
	v_mfma_f32_32x32x16_bf16 v[66:81], v[174:177], v[98:101], v[66:81]
	s_waitcnt lgkmcnt(0)
	v_mfma_f32_32x32x16_bf16 v[34:49], v[178:181], v[98:101], v[34:49]
	ds_read_b128 v[174:177], v173 offset:24576
	ds_read_b128 v[178:181], v173 offset:32768
	v_add_u32_e32 v173, s6, v161
	s_waitcnt lgkmcnt(1)
	v_mfma_f32_32x32x16_bf16 v[66:81], v[174:177], v[94:97], v[66:81]
	s_waitcnt lgkmcnt(0)
	v_mfma_f32_32x32x16_bf16 v[34:49], v[178:181], v[94:97], v[34:49]
	ds_read_b128 v[174:177], v173 offset:24576
	ds_read_b128 v[178:181], v173 offset:32768
	v_add_u32_e32 v173, s6, v160
	s_waitcnt lgkmcnt(1)
	v_mfma_f32_32x32x16_bf16 v[66:81], v[174:177], v[90:93], v[66:81]
	s_waitcnt lgkmcnt(0)
	v_mfma_f32_32x32x16_bf16 v[34:49], v[178:181], v[90:93], v[34:49]
	ds_read_b128 v[174:177], v173 offset:24576
	ds_read_b128 v[178:181], v173 offset:32768
	s_waitcnt lgkmcnt(1)
	v_mfma_f32_32x32x16_bf16 v[66:81], v[174:177], v[86:89], v[66:81]
	v_exp_f32_e32 v175, v50
	v_add_f32_e32 v50, 0, v222
	v_add_f32_e32 v50, v223, v50
	v_add_f32_e32 v50, v227, v50
	v_add_f32_e32 v50, v230, v50
	v_add_f32_e32 v50, v231, v50
	v_add_f32_e32 v50, v232, v50
	v_add_f32_e32 v50, v233, v50
	v_add_f32_e32 v50, v234, v50
	v_add_f32_e32 v50, v235, v50
	v_add_f32_e32 v50, v236, v50
	v_add_f32_e32 v50, v237, v50
	v_add_f32_e32 v50, v238, v50
	v_add_f32_e32 v50, v239, v50
	v_exp_f32_e32 v176, v51
	v_add_f32_e32 v50, v240, v50
	v_exp_f32_e32 v177, v52
	v_add_f32_e32 v50, v241, v50
	s_waitcnt lgkmcnt(0)
	v_mfma_f32_32x32x16_bf16 v[34:49], v[178:181], v[86:89], v[34:49]
	v_lshl_add_u32 v247, s10, 13, v158
	ds_read_b64_tr_b16 v[206:207], v247 offset:0
	ds_read_b64_tr_b16 v[208:209], v247 offset:0x400
	ds_read_b64_tr_b16 v[210:211], v247 offset:0x800
	ds_read_b64_tr_b16 v[212:213], v247 offset:0xc00
	ds_read_b64_tr_b16 v[214:215], v247 offset:0x1000
	ds_read_b64_tr_b16 v[216:217], v247 offset:0x1400
	ds_read_b64_tr_b16 v[218:219], v247 offset:0x1800
	ds_read_b64_tr_b16 v[220:221], v247 offset:0x1c00
	v_exp_f32_e32 v178, v53
	v_add_f32_e32 v50, v246, v50
	v_exp_f32_e32 v179, v54
	v_add_f32_e32 v50, v175, v50
	v_exp_f32_e32 v180, v55
	v_add_f32_e32 v50, v176, v50
	v_exp_f32_e32 v181, v56
	v_add_f32_e32 v50, v177, v50
	v_add_f32_e32 v50, v178, v50
	v_add_f32_e32 v50, v179, v50
	v_add_f32_e32 v50, v180, v50
	v_add_f32_e32 v50, v181, v50
	v_add_f32_e32 v50, v198, v50
	v_add_f32_e32 v50, v199, v50
	v_add_f32_e32 v50, v200, v50
	v_mfma_f32_32x32x16_bf16 v[66:81], v[82:85], v[110:113], v[66:81]
	v_add_f32_e32 v50, v201, v50
	v_add_f32_e32 v50, v202, v50
	v_add_f32_e32 v50, v203, v50
	v_add_f32_e32 v50, v204, v50
	v_add_f32_e32 v50, v205, v50
	v_add_f32_e32 v173, v65, v50
	v_mfma_f32_32x32x16_bf16 v[34:49], v[82:85], v[110:113], v[34:49]
	v_cvt_pk_bf16_f32 v50, v222, v223
	v_cvt_pk_bf16_f32 v51, v227, v230
	v_cvt_pk_bf16_f32 v52, v231, v232
	v_cvt_pk_bf16_f32 v53, v233, v234
	v_cvt_pk_bf16_f32 v54, v235, v236
	v_cvt_pk_bf16_f32 v55, v237, v238
	v_cvt_pk_bf16_f32 v56, v239, v240
	v_cvt_pk_bf16_f32 v57, v241, v246
	v_cvt_pk_bf16_f32 v58, v175, v176
	v_cvt_pk_bf16_f32 v59, v177, v178
	v_cvt_pk_bf16_f32 v60, v179, v180
	v_cvt_pk_bf16_f32 v61, v181, v198
	v_cvt_pk_bf16_f32 v62, v199, v200
	v_cvt_pk_bf16_f32 v63, v201, v202
	v_cvt_pk_bf16_f32 v64, v203, v204
	v_cvt_pk_bf16_f32 v65, v205, v65
	s_cmp_ge_u32 s8, s19
	s_cselect_b64 s[4:5], -1, 0
	s_and_b64 vcc, exec, s[4:5]
	s_cbranch_vccnz .Lattn_h2_noload
	global_load_dwordx4 v[114:117], v146, s[84:85]
	global_load_dwordx4 v[118:121], v144, s[82:83]
	global_load_dwordx4 v[122:125], v142, s[82:83]
	s_add_u32 s82, s82, 0x3000
	s_addc_u32 s83, s83, 0
	s_add_u32 s84, s84, 0x2000
	s_addc_u32 s85, s85, 0
.LBB0_1439:
	s_waitcnt lgkmcnt(0)
	s_nop 0
	v_mfma_f32_32x32x16_bf16 v[2:17], v[50:53], v[206:209], v[2:17]
	ds_read_b64_tr_b16 v[148:149], v247 offset:0x200
	ds_read_b64_tr_b16 v[150:151], v247 offset:0x600
	v_max_f32_e32 v249, v67, v67
	v_max_f32_e32 v248, v66, v66
	v_max_f32_e32 v248, v248, v249
	v_max3_f32 v248, v248, v68, v69
	v_max3_f32 v248, v248, v70, v71
	v_mfma_f32_32x32x16_bf16 v[2:17], v[54:57], v[210:213], v[2:17]
	ds_read_b64_tr_b16 v[176:177], v247 offset:0xa00
	ds_read_b64_tr_b16 v[178:179], v247 offset:0xe00
	v_max3_f32 v248, v248, v72, v73
	v_max3_f32 v248, v248, v74, v75
	v_max3_f32 v248, v248, v76, v77
	v_max3_f32 v248, v248, v78, v79
	v_mfma_f32_32x32x16_bf16 v[2:17], v[58:61], v[214:217], v[2:17]
	ds_read_b64_tr_b16 v[180:181], v247 offset:0x1200
	ds_read_b64_tr_b16 v[182:183], v247 offset:0x1600
	v_max3_f32 v248, v248, v80, v81
	v_max3_f32 v248, v248, v34, v35
	v_max3_f32 v248, v248, v36, v37
	v_max3_f32 v248, v248, v38, v39
	v_mfma_f32_32x32x16_bf16 v[2:17], v[62:65], v[218:221], v[2:17]
	ds_read_b64_tr_b16 v[184:185], v247 offset:0x1a00
	ds_read_b64_tr_b16 v[186:187], v247 offset:0x1e00
	v_max3_f32 v248, v248, v40, v41
	v_max3_f32 v248, v248, v42, v43
	v_max3_f32 v248, v248, v44, v45
	v_max3_f32 v248, v248, v46, v47
	v_max3_f32 v248, v248, v48, v49
	s_add_i32 s6, s9, 1
	s_cmp_lg_u32 s9, 2
	s_cselect_b32 s10, s6, 0
	s_lshl_b32 s20, s10, 13
	s_lshl_b32 s6, s10, 14
	s_add_i32 s21, s6, 0
	s_waitcnt vmcnt(3)
	v_add_u32_e32 v247, s20, v165
	ds_write_b128 v247, v[130:133]
	v_add_u32_e32 v247, s21, v163
	ds_write_b128 v247, v[126:129] offset:24576
	v_add_u32_e32 v247, s21, v164
	ds_write_b128 v247, v[134:137] offset:24576
	s_waitcnt lgkmcnt(3)
	v_mfma_f32_32x32x16_bf16 v[18:33], v[50:53], v[148:151], v[18:33]
	v_exp_f32_e32 v222, v66
	v_exp_f32_e32 v223, v67
	v_exp_f32_e32 v227, v68
	v_exp_f32_e32 v230, v69
	v_mfma_f32_32x32x16_bf16 v[18:33], v[54:57], v[176:179], v[18:33]
	v_exp_f32_e32 v231, v70
	v_exp_f32_e32 v232, v71
	v_exp_f32_e32 v233, v72
	v_exp_f32_e32 v234, v73
	v_mfma_f32_32x32x16_bf16 v[18:33], v[58:61], v[180:183], v[18:33]
	v_exp_f32_e32 v235, v74
	v_exp_f32_e32 v236, v75
	v_exp_f32_e32 v237, v76
	v_exp_f32_e32 v238, v77
	v_mfma_f32_32x32x16_bf16 v[18:33], v[62:65], v[184:187], v[18:33]
	v_exp_f32_e32 v239, v78
	v_exp_f32_e32 v240, v79
	v_exp_f32_e32 v241, v80
	v_exp_f32_e32 v246, v81
	s_mov_b32 s6, 0x41380000
	v_cmp_ge_f32_e32 vcc, s6, v248
	s_cmp_eq_u64 vcc, exec
	v_mov_b32_e32 v148, 1.0
	s_cbranch_scc0 .LBB0_1449
.LBB0_1446:
	s_add_i32 s6, s10, 1
	s_cmp_lg_u32 s10, 2
	v_fmac_f32_e32 v170, v169, v157
	s_cselect_b32 s22, s6, 0
	v_fmac_f32_e32 v173, v170, v172
	v_mov_b32_e32 v157, v173
	s_add_i32 s8, s8, 2
	s_and_b64 vcc, exec, s[4:5]
	s_waitcnt lgkmcnt(0)
	s_barrier
	s_cbranch_vccnz .LBB0_1450
	v_mov_b32_e32 v169, v148
	s_branch .LBB0_1429
.LBB0_1448:
	v_mov_b32_e32 v249, v248
	s_nop 1
	v_permlane32_swap_b32_e32 v248, v249
	v_max_f32_e32 v249, v249, v249
	v_max_f32_e32 v248, v248, v248
	v_max_f32_e32 v34, v248, v249
	v_max_f32_e32 v34, v34, v34
	v_max_f32_e32 v34, 0, v34
	v_add_f32_e32 v34, v159, v34
	v_cvt_pk_bf16_f32 v34, v34, v83
	s_nop 0
	v_lshlrev_b32_e32 v35, 16, v34
	v_sub_f32_e32 v34, v35, v159
	v_exp_f32_e64 v172, -v34
	v_pk_add_f32 v[66:67], v[66:67], v[34:35] op_sel_hi:[1,0] neg_lo:[0,1] neg_hi:[0,1]
	v_pk_add_f32 v[68:69], v[68:69], v[34:35] op_sel_hi:[1,0] neg_lo:[0,1] neg_hi:[0,1]
	v_pk_add_f32 v[70:71], v[70:71], v[34:35] op_sel_hi:[1,0] neg_lo:[0,1] neg_hi:[0,1]
	v_pk_add_f32 v[72:73], v[72:73], v[34:35] op_sel_hi:[1,0] neg_lo:[0,1] neg_hi:[0,1]
	v_pk_add_f32 v[74:75], v[74:75], v[34:35] op_sel_hi:[1,0] neg_lo:[0,1] neg_hi:[0,1]
	v_pk_add_f32 v[76:77], v[76:77], v[34:35] op_sel_hi:[1,0] neg_lo:[0,1] neg_hi:[0,1]
	v_pk_add_f32 v[78:79], v[78:79], v[34:35] op_sel_hi:[1,0] neg_lo:[0,1] neg_hi:[0,1]
	v_pk_add_f32 v[80:81], v[80:81], v[34:35] op_sel_hi:[1,0] neg_lo:[0,1] neg_hi:[0,1]
	v_sub_f32_e32 v65, v65, v34
	v_sub_f32_e32 v64, v64, v34
	v_sub_f32_e32 v63, v63, v34
	v_sub_f32_e32 v62, v62, v34
	v_sub_f32_e32 v61, v61, v34
	v_sub_f32_e32 v60, v60, v34
	v_sub_f32_e32 v59, v59, v34
	v_sub_f32_e32 v58, v58, v34
	v_sub_f32_e32 v57, v57, v34
	v_sub_f32_e32 v56, v56, v34
	v_sub_f32_e32 v55, v55, v34
	v_sub_f32_e32 v54, v54, v34
	v_sub_f32_e32 v53, v53, v34
	v_sub_f32_e32 v52, v52, v34
	v_sub_f32_e32 v51, v51, v34
	v_sub_f32_e32 v50, v50, v34
	v_exp_f32_e32 v222, v66
	v_exp_f32_e32 v223, v67
	v_exp_f32_e32 v227, v68
	v_exp_f32_e32 v230, v69
	v_exp_f32_e32 v231, v70
	v_exp_f32_e32 v232, v71
	v_exp_f32_e32 v233, v72
	v_exp_f32_e32 v234, v73
	v_exp_f32_e32 v235, v74
	v_exp_f32_e32 v236, v75
	v_exp_f32_e32 v237, v76
	v_exp_f32_e32 v238, v77
	v_exp_f32_e32 v239, v78
	v_exp_f32_e32 v240, v79
	v_exp_f32_e32 v241, v80
	v_exp_f32_e32 v246, v81
	v_mov_b32_e32 v159, v35
	s_branch .LBB0_1431
.LBB0_1449:
	v_mov_b32_e32 v249, v248
	s_nop 1
	v_permlane32_swap_b32_e32 v248, v249
	v_max_f32_e32 v249, v249, v249
	v_max_f32_e32 v248, v248, v248
	v_max_f32_e32 v50, v248, v249
	v_max_f32_e32 v50, v50, v50
	v_max_f32_e32 v50, 0, v50
	v_add_f32_e32 v50, v159, v50
	v_cvt_pk_bf16_f32 v50, v50, v83
	s_nop 0
	v_lshlrev_b32_e32 v51, 16, v50
	v_sub_f32_e32 v50, v51, v159
	v_exp_f32_e64 v148, -v50
	v_pk_add_f32 v[66:67], v[66:67], v[50:51] op_sel_hi:[1,0] neg_lo:[0,1] neg_hi:[0,1]
	v_pk_add_f32 v[68:69], v[68:69], v[50:51] op_sel_hi:[1,0] neg_lo:[0,1] neg_hi:[0,1]
	v_pk_add_f32 v[70:71], v[70:71], v[50:51] op_sel_hi:[1,0] neg_lo:[0,1] neg_hi:[0,1]
	v_pk_add_f32 v[72:73], v[72:73], v[50:51] op_sel_hi:[1,0] neg_lo:[0,1] neg_hi:[0,1]
	v_pk_add_f32 v[74:75], v[74:75], v[50:51] op_sel_hi:[1,0] neg_lo:[0,1] neg_hi:[0,1]
	v_pk_add_f32 v[76:77], v[76:77], v[50:51] op_sel_hi:[1,0] neg_lo:[0,1] neg_hi:[0,1]
	v_pk_add_f32 v[78:79], v[78:79], v[50:51] op_sel_hi:[1,0] neg_lo:[0,1] neg_hi:[0,1]
	v_pk_add_f32 v[80:81], v[80:81], v[50:51] op_sel_hi:[1,0] neg_lo:[0,1] neg_hi:[0,1]
	v_sub_f32_e32 v49, v49, v50
	v_sub_f32_e32 v48, v48, v50
	v_sub_f32_e32 v47, v47, v50
	v_sub_f32_e32 v46, v46, v50
	v_sub_f32_e32 v45, v45, v50
	v_sub_f32_e32 v44, v44, v50
	v_sub_f32_e32 v43, v43, v50
	v_sub_f32_e32 v42, v42, v50
	v_sub_f32_e32 v41, v41, v50
	v_sub_f32_e32 v40, v40, v50
	v_sub_f32_e32 v39, v39, v50
	v_sub_f32_e32 v38, v38, v50
	v_sub_f32_e32 v37, v37, v50
	v_sub_f32_e32 v36, v36, v50
	v_sub_f32_e32 v35, v35, v50
	v_sub_f32_e32 v34, v34, v50
	v_exp_f32_e32 v222, v66
	v_exp_f32_e32 v223, v67
	v_exp_f32_e32 v227, v68
	v_exp_f32_e32 v230, v69
	v_exp_f32_e32 v231, v70
	v_exp_f32_e32 v232, v71
	v_exp_f32_e32 v233, v72
	v_exp_f32_e32 v234, v73
	v_exp_f32_e32 v235, v74
	v_exp_f32_e32 v236, v75
	v_exp_f32_e32 v237, v76
	v_exp_f32_e32 v238, v77
	v_exp_f32_e32 v239, v78
	v_exp_f32_e32 v240, v79
	v_exp_f32_e32 v241, v80
	v_exp_f32_e32 v246, v81
	v_mov_b32_e32 v159, v51
	s_branch .LBB0_1440

.LBB0_1436:
	s_or_b64 exec, exec, s[4:5]
	s_waitcnt lgkmcnt(0)
	v_pk_mul_f32 v[14:15], v[14:15], v[46:47]
	v_pk_mul_f32 v[10:11], v[10:11], v[42:43]
	v_pk_mul_f32 v[6:7], v[6:7], v[38:39]
	v_pk_mul_f32 v[16:17], v[16:17], v[48:49]
	v_pk_mul_f32 v[12:13], v[12:13], v[44:45]
	v_pk_mul_f32 v[8:9], v[8:9], v[40:41]
	v_pk_mul_f32 v[4:5], v[4:5], v[36:37]
	v_pk_mul_f32 v[2:3], v[2:3], v[34:35]
	v_pk_mul_f32 v[30:31], v[30:31], v[46:47]
	v_pk_mul_f32 v[26:27], v[26:27], v[42:43]
	v_pk_mul_f32 v[22:23], v[22:23], v[38:39]
	v_pk_mul_f32 v[32:33], v[32:33], v[48:49]
	v_pk_mul_f32 v[28:29], v[28:29], v[44:45]
	v_pk_mul_f32 v[24:25], v[24:25], v[40:41]
	v_pk_mul_f32 v[20:21], v[20:21], v[36:37]
	v_pk_mul_f32 v[18:19], v[18:19], v[34:35]
	s_branch .LBB0_1437

.LBB0_1445:
	s_or_b64 exec, exec, s[6:7]
	s_waitcnt lgkmcnt(0)
	v_pk_mul_f32 v[14:15], v[14:15], v[62:63]
	v_pk_mul_f32 v[10:11], v[10:11], v[58:59]
	v_pk_mul_f32 v[6:7], v[6:7], v[54:55]
	v_pk_mul_f32 v[16:17], v[16:17], v[64:65]
	v_pk_mul_f32 v[12:13], v[12:13], v[60:61]
	v_pk_mul_f32 v[8:9], v[8:9], v[56:57]
	v_pk_mul_f32 v[4:5], v[4:5], v[52:53]
	v_pk_mul_f32 v[2:3], v[2:3], v[50:51]
	v_pk_mul_f32 v[30:31], v[30:31], v[62:63]
	v_pk_mul_f32 v[26:27], v[26:27], v[58:59]
	v_pk_mul_f32 v[22:23], v[22:23], v[54:55]
	v_pk_mul_f32 v[32:33], v[32:33], v[64:65]
	v_pk_mul_f32 v[28:29], v[28:29], v[60:61]
	v_pk_mul_f32 v[24:25], v[24:25], v[56:57]
	v_pk_mul_f32 v[20:21], v[20:21], v[52:53]
	v_pk_mul_f32 v[18:19], v[18:19], v[50:51]
	s_branch .LBB0_1446

.LBB0_1450:
	v_mov_b32_e32 v249, v157
	s_nop 1
	v_permlane32_swap_b32_e32 v157, v249
	v_add_f32_e32 v157, v157, v249
	v_add_u32_e32 v54, s21, v167
	ds_read_b128 v[50:53], v54 offset:24576
	ds_read_b128 v[54:57], v54 offset:32768
	v_add_u32_e32 v114, s21, v168
	v_exp_f32_e32 v49, v49
	s_waitcnt lgkmcnt(1)
	v_mfma_f32_32x32x16_bf16 v[66:81], v[50:53], v[106:109], 0
	s_waitcnt lgkmcnt(0)
	v_mfma_f32_32x32x16_bf16 v[50:65], v[54:57], v[106:109], 0
	ds_read_b128 v[106:109], v114 offset:24576
	ds_read_b128 v[114:117], v114 offset:32768
	s_waitcnt lgkmcnt(1)
	v_mfma_f32_32x32x16_bf16 v[66:81], v[106:109], v[102:105], v[66:81]
	v_add_u32_e32 v106, s21, v166
	s_waitcnt lgkmcnt(0)
	v_mfma_f32_32x32x16_bf16 v[50:65], v[114:117], v[102:105], v[50:65]
	ds_read_b128 v[102:105], v106 offset:24576
	ds_read_b128 v[106:109], v106 offset:32768
	s_waitcnt lgkmcnt(1)
	v_mfma_f32_32x32x16_bf16 v[66:81], v[102:105], v[98:101], v[66:81]
	v_add_u32_e32 v102, s21, v162
	s_waitcnt lgkmcnt(0)
	v_mfma_f32_32x32x16_bf16 v[50:65], v[106:109], v[98:101], v[50:65]
	ds_read_b128 v[98:101], v102 offset:24576
	ds_read_b128 v[102:105], v102 offset:32768
	s_waitcnt lgkmcnt(1)
	v_mfma_f32_32x32x16_bf16 v[66:81], v[98:101], v[94:97], v[66:81]
	v_add_u32_e32 v98, s21, v161
	s_waitcnt lgkmcnt(0)
	v_mfma_f32_32x32x16_bf16 v[50:65], v[102:105], v[94:97], v[50:65]
	ds_read_b128 v[94:97], v98 offset:24576
	ds_read_b128 v[98:101], v98 offset:32768
	s_waitcnt lgkmcnt(1)
	v_mfma_f32_32x32x16_bf16 v[66:81], v[94:97], v[90:93], v[66:81]
	v_add_u32_e32 v94, s21, v160
	s_waitcnt lgkmcnt(0)
	v_mfma_f32_32x32x16_bf16 v[50:65], v[98:101], v[90:93], v[50:65]
	ds_read_b128 v[90:93], v94 offset:24576
	ds_read_b128 v[94:97], v94 offset:32768
	v_exp_f32_e32 v98, v47
	v_exp_f32_e32 v99, v48
	s_waitcnt lgkmcnt(1)
	v_mfma_f32_32x32x16_bf16 v[66:81], v[90:93], v[86:89], v[66:81]
	v_exp_f32_e32 v90, v39
	v_exp_f32_e32 v91, v40
	v_exp_f32_e32 v92, v41
	v_exp_f32_e32 v93, v42
	s_waitcnt lgkmcnt(0)
	v_mfma_f32_32x32x16_bf16 v[50:65], v[94:97], v[86:89], v[50:65]
	v_exp_f32_e32 v86, v35
	v_exp_f32_e32 v87, v36
	v_exp_f32_e32 v88, v37
	v_exp_f32_e32 v89, v38
	v_exp_f32_e32 v94, v43
	v_exp_f32_e32 v95, v44
	v_exp_f32_e32 v96, v45
	v_mfma_f32_32x32x16_bf16 v[66:81], v[82:85], v[110:113], v[66:81]
	v_exp_f32_e32 v97, v46
	v_mfma_f32_32x32x16_bf16 v[50:65], v[82:85], v[110:113], v[50:65]
	v_exp_f32_e32 v85, v34
	v_add_f32_e32 v34, 0, v222
	v_add_f32_e32 v34, v223, v34
	v_add_f32_e32 v34, v227, v34
	v_add_f32_e32 v34, v230, v34
	v_add_f32_e32 v34, v231, v34
	v_add_f32_e32 v34, v232, v34
	v_add_f32_e32 v34, v233, v34
	v_add_f32_e32 v34, v234, v34
	v_add_f32_e32 v34, v235, v34
	v_add_f32_e32 v34, v236, v34
	v_add_f32_e32 v34, v237, v34
	v_add_f32_e32 v34, v238, v34
	v_add_f32_e32 v34, v239, v34
	v_add_f32_e32 v34, v240, v34
	v_add_f32_e32 v34, v241, v34
	v_add_f32_e32 v34, v246, v34
	v_add_f32_e32 v34, v85, v34
	v_add_f32_e32 v34, v86, v34
	v_add_f32_e32 v34, v87, v34
	v_add_f32_e32 v34, v88, v34
	v_add_f32_e32 v34, v89, v34
	v_add_f32_e32 v34, v90, v34
	v_add_f32_e32 v34, v91, v34
	v_add_f32_e32 v34, v92, v34
	v_add_f32_e32 v34, v93, v34
	v_add_f32_e32 v34, v94, v34
	v_add_f32_e32 v34, v95, v34
	v_add_f32_e32 v34, v96, v34
	v_add_f32_e32 v34, v97, v34
	v_add_f32_e32 v34, v98, v34
	v_add_f32_e32 v34, v99, v34
	v_add_f32_e32 v82, v49, v34
	v_mov_b32_e32 v84, v82
	v_cvt_pk_bf16_f32 v34, v222, v223
	v_cvt_pk_bf16_f32 v35, v227, v230
	v_cvt_pk_bf16_f32 v36, v231, v232
	s_nop 1
	v_permlane32_swap_b32_e32 v82, v84
	v_cvt_pk_bf16_f32 v37, v233, v234
	v_cvt_pk_bf16_f32 v38, v235, v236
	v_cvt_pk_bf16_f32 v39, v237, v238
	v_cvt_pk_bf16_f32 v40, v239, v240
	v_cvt_pk_bf16_f32 v41, v241, v246
	v_cvt_pk_bf16_f32 v42, v85, v86
	v_cvt_pk_bf16_f32 v43, v87, v88
	v_cvt_pk_bf16_f32 v44, v89, v90
	v_cvt_pk_bf16_f32 v45, v91, v92
	v_cvt_pk_bf16_f32 v46, v93, v94
	v_cvt_pk_bf16_f32 v47, v95, v96
	v_cvt_pk_bf16_f32 v48, v97, v98
	v_cvt_pk_bf16_f32 v49, v99, v49
	v_add_u32_e32 v85, s11, v158
	ds_read_b64_tr_b16 v[86:87], v85 offset:0
	ds_read_b64_tr_b16 v[88:89], v85 offset:0x400
	ds_read_b64_tr_b16 v[90:91], v85 offset:0x800
	ds_read_b64_tr_b16 v[92:93], v85 offset:0xc00
	ds_read_b64_tr_b16 v[94:95], v85 offset:0x1000
	ds_read_b64_tr_b16 v[96:97], v85 offset:0x1400
	ds_read_b64_tr_b16 v[98:99], v85 offset:0x1800
	ds_read_b64_tr_b16 v[100:101], v85 offset:0x1c00
	s_waitcnt lgkmcnt(0)
	s_nop 0
	v_mfma_f32_32x32x16_bf16 v[2:17], v[34:37], v[86:89], v[2:17]
	ds_read_b64_tr_b16 v[86:87], v85 offset:0x200
	ds_read_b64_tr_b16 v[88:89], v85 offset:0x600
	v_mfma_f32_32x32x16_bf16 v[2:17], v[38:41], v[90:93], v[2:17]
	ds_read_b64_tr_b16 v[90:91], v85 offset:0xa00
	ds_read_b64_tr_b16 v[92:93], v85 offset:0xe00
	v_mfma_f32_32x32x16_bf16 v[2:17], v[42:45], v[94:97], v[2:17]
	ds_read_b64_tr_b16 v[94:95], v85 offset:0x1200
	ds_read_b64_tr_b16 v[96:97], v85 offset:0x1600
	v_mfma_f32_32x32x16_bf16 v[2:17], v[46:49], v[98:101], v[2:17]
	ds_read_b64_tr_b16 v[98:99], v85 offset:0x1a00
	ds_read_b64_tr_b16 v[100:101], v85 offset:0x1e00
	s_waitcnt lgkmcnt(0)
	v_mfma_f32_32x32x16_bf16 v[18:33], v[34:37], v[86:89], v[18:33]
	v_max_f32_e32 v34, v67, v67
	v_max_f32_e32 v35, v66, v66
	v_max_f32_e32 v34, v35, v34
	v_max3_f32 v34, v34, v68, v69
	v_max3_f32 v34, v34, v70, v71
	v_max3_f32 v34, v34, v72, v73
	v_max3_f32 v34, v34, v74, v75
	v_mfma_f32_32x32x16_bf16 v[18:33], v[38:41], v[90:93], v[18:33]
	v_max3_f32 v34, v34, v76, v77
	v_max3_f32 v34, v34, v78, v79
	v_max3_f32 v34, v34, v80, v81
	v_max3_f32 v34, v34, v50, v51
	v_max3_f32 v34, v34, v52, v53
	v_max3_f32 v34, v34, v54, v55
	v_max3_f32 v34, v34, v56, v57
	v_mfma_f32_32x32x16_bf16 v[18:33], v[42:45], v[94:97], v[18:33]
	v_max3_f32 v34, v34, v58, v59
	v_max3_f32 v34, v34, v60, v61
	v_max3_f32 v34, v34, v62, v63
	v_max3_f32 v34, v34, v64, v65
	v_mov_b32_e32 v35, v34
	s_nop 1
	v_permlane32_swap_b32_e32 v34, v35
	v_mfma_f32_32x32x16_bf16 v[18:33], v[46:49], v[98:101], v[18:33]
	v_max_f32_e32 v35, v35, v35
	v_max_f32_e32 v34, v34, v34
	v_max_f32_e32 v34, v34, v35
	s_mov_b32 s4, 0x41380000
	v_cmp_ge_f32_e32 vcc, s4, v34
	s_cmp_eq_u64 vcc, exec
	v_mov_b32_e32 v85, 1.0
	s_cbranch_scc0 .LBB0_1462
	v_cmp_gt_f32_e32 vcc, 1.0, v85
	s_cbranch_vccz .LBB0_1457

.LBB0_1457:
	v_exp_f32_e32 v36, v66
	v_exp_f32_e32 v37, v67
	v_exp_f32_e32 v38, v68
	v_exp_f32_e32 v39, v69
	v_exp_f32_e32 v40, v70
	v_add_f32_e32 v34, 0, v36
	v_exp_f32_e32 v41, v71
	v_add_f32_e32 v34, v37, v34
	v_exp_f32_e32 v42, v72
	v_add_f32_e32 v34, v38, v34
	v_exp_f32_e32 v43, v73
	v_add_f32_e32 v34, v39, v34
	v_exp_f32_e32 v44, v74
	v_add_f32_e32 v34, v40, v34
	v_exp_f32_e32 v45, v75
	v_add_f32_e32 v34, v41, v34
	v_exp_f32_e32 v46, v76
	v_add_f32_e32 v34, v42, v34
	v_exp_f32_e32 v47, v77
	v_add_f32_e32 v34, v43, v34
	v_exp_f32_e32 v48, v78
	v_add_f32_e32 v34, v44, v34
	v_exp_f32_e32 v49, v79
	v_add_f32_e32 v34, v45, v34
	v_exp_f32_e32 v66, v80
	v_add_f32_e32 v34, v46, v34
	v_exp_f32_e32 v67, v81
	v_add_f32_e32 v34, v47, v34
	v_exp_f32_e32 v50, v50
	v_add_f32_e32 v34, v48, v34
	v_exp_f32_e32 v51, v51
	v_add_f32_e32 v34, v49, v34
	v_exp_f32_e32 v52, v52
	v_add_f32_e32 v34, v66, v34
	v_exp_f32_e32 v53, v53
	v_add_f32_e32 v34, v67, v34
	v_exp_f32_e32 v54, v54
	v_add_f32_e32 v34, v50, v34
	v_exp_f32_e32 v55, v55
	v_add_f32_e32 v34, v51, v34
	v_exp_f32_e32 v56, v56
	v_add_f32_e32 v34, v52, v34
	v_exp_f32_e32 v57, v57
	v_add_f32_e32 v34, v53, v34
	v_exp_f32_e32 v58, v58
	v_add_f32_e32 v34, v54, v34
	v_exp_f32_e32 v59, v59
	v_add_f32_e32 v34, v55, v34
	v_exp_f32_e32 v60, v60
	v_add_f32_e32 v34, v56, v34
	v_exp_f32_e32 v61, v61
	v_add_f32_e32 v34, v57, v34
	v_exp_f32_e32 v62, v62
	v_add_f32_e32 v34, v58, v34
	v_exp_f32_e32 v63, v63
	v_add_f32_e32 v34, v59, v34
	v_exp_f32_e32 v64, v64
	v_add_f32_e32 v34, v60, v34
	v_exp_f32_e32 v65, v65
	v_add_f32_e32 v34, v61, v34
	v_add_f32_e32 v34, v62, v34
	v_add_f32_e32 v34, v63, v34
	v_add_f32_e32 v34, v64, v34
	v_add_f32_e32 v34, v65, v34
	v_mov_b32_e32 v35, v34
	s_nop 1
	v_permlane32_swap_b32_e32 v34, v35
	v_cvt_pk_bf16_f32 v36, v36, v37
	v_cvt_pk_bf16_f32 v37, v38, v39
	v_cvt_pk_bf16_f32 v38, v40, v41
	v_cvt_pk_bf16_f32 v39, v42, v43
	v_cvt_pk_bf16_f32 v40, v44, v45
	v_cvt_pk_bf16_f32 v41, v46, v47
	v_cvt_pk_bf16_f32 v42, v48, v49
	v_cvt_pk_bf16_f32 v43, v66, v67
	v_cvt_pk_bf16_f32 v44, v50, v51
	v_cvt_pk_bf16_f32 v45, v52, v53
	v_cvt_pk_bf16_f32 v46, v54, v55
	v_cvt_pk_bf16_f32 v47, v56, v57
	v_cvt_pk_bf16_f32 v48, v58, v59
	v_cvt_pk_bf16_f32 v49, v60, v61
	v_cvt_pk_bf16_f32 v50, v62, v63
	v_cvt_pk_bf16_f32 v51, v64, v65
	s_nop 0
	v_add_u32_e32 v68, s20, v158
	ds_read_b64_tr_b16 v[52:53], v68 offset:0
	ds_read_b64_tr_b16 v[54:55], v68 offset:0x400
	ds_read_b64_tr_b16 v[56:57], v68 offset:0x800
	ds_read_b64_tr_b16 v[58:59], v68 offset:0xc00
	ds_read_b64_tr_b16 v[60:61], v68 offset:0x1000
	ds_read_b64_tr_b16 v[62:63], v68 offset:0x1400
	ds_read_b64_tr_b16 v[64:65], v68 offset:0x1800
	ds_read_b64_tr_b16 v[66:67], v68 offset:0x1c00
	s_waitcnt lgkmcnt(0)
	s_nop 0
	v_mfma_f32_32x32x16_bf16 v[2:17], v[36:39], v[52:55], v[2:17]
	ds_read_b64_tr_b16 v[52:53], v68 offset:0x200
	ds_read_b64_tr_b16 v[54:55], v68 offset:0x600
	v_mfma_f32_32x32x16_bf16 v[2:17], v[40:43], v[56:59], v[2:17]
	ds_read_b64_tr_b16 v[56:57], v68 offset:0xa00
	ds_read_b64_tr_b16 v[58:59], v68 offset:0xe00
	v_mfma_f32_32x32x16_bf16 v[2:17], v[44:47], v[60:63], v[2:17]
	ds_read_b64_tr_b16 v[60:61], v68 offset:0x1200
	ds_read_b64_tr_b16 v[62:63], v68 offset:0x1600
	v_mfma_f32_32x32x16_bf16 v[2:17], v[48:51], v[64:67], v[2:17]
	ds_read_b64_tr_b16 v[64:65], v68 offset:0x1a00
	ds_read_b64_tr_b16 v[66:67], v68 offset:0x1e00
	s_waitcnt lgkmcnt(0)
	v_mfma_f32_32x32x16_bf16 v[18:33], v[36:39], v[52:55], v[18:33]
	v_mfma_f32_32x32x16_bf16 v[18:33], v[40:43], v[56:59], v[18:33]
	v_mfma_f32_32x32x16_bf16 v[18:33], v[44:47], v[60:63], v[18:33]
	v_mfma_f32_32x32x16_bf16 v[18:33], v[48:51], v[64:67], v[18:33]
	s_and_saveexec_b64 s[4:5], s[0:1]
	v_add_f32_e32 v36, v82, v84
	v_fmac_f32_e32 v36, v157, v148
	v_add_f32_e32 v34, v34, v35
	v_fmac_f32_e32 v34, v36, v85
	ds_write_b32 v156, v34
	s_or_b64 exec, exec, s[4:5]
	s_waitcnt lgkmcnt(0)
	v_add_u32_e32 v42, v141, v138
	ds_read_b128 v[34:37], v42
	ds_read_b128 v[38:41], v42 offset:32
	s_lshl_b64 s[0:1], s[2:3], 11
	v_readlane_b32 s2, v253, 13
	v_readlane_b32 s3, v253, 14
	s_add_u32 s2, s2, s0
	s_waitcnt lgkmcnt(1)
	v_rcp_f32_e32 v43, v34
	v_rcp_f32_e32 v44, v35
	v_rcp_f32_e32 v45, v36
	v_rcp_f32_e32 v46, v37
	ds_read_b128 v[34:37], v42 offset:64
	s_addc_u32 s3, s3, s1
	s_lshl_b32 s0, s18, 6
	s_ashr_i32 s1, s0, 31
	s_lshl_b64 s[0:1], s[0:1], 1
	s_add_u32 s0, s2, s0
	s_waitcnt lgkmcnt(1)
	v_rcp_f32_e32 v47, v38
	v_rcp_f32_e32 v48, v39
	v_rcp_f32_e32 v49, v40
	v_rcp_f32_e32 v50, v41
	ds_read_b128 v[38:41], v42 offset:96
	v_ashrrev_i32_e32 v141, 31, v140
	s_addc_u32 s1, s3, s1
	s_waitcnt lgkmcnt(1)
	v_rcp_f32_e32 v42, v34
	v_rcp_f32_e32 v51, v35
	v_lshlrev_b64 v[34:35], 11, v[140:141]
	v_lshl_add_u64 v[34:35], s[0:1], 0, v[34:35]
	v_lshlrev_b32_e32 v82, 1, v139
	v_rcp_f32_e32 v52, v36
	v_rcp_f32_e32 v53, v37
	v_lshlrev_b32_e32 v36, 13, v155
	v_lshl_add_u64 v[34:35], v[34:35], 0, v[82:83]
	v_mov_b32_e32 v37, v83
	v_lshl_add_u64 v[34:35], v[34:35], 0, v[36:37]
	s_mov_b64 s[0:1], 0x25bb0300
	v_mul_f32_e32 v2, v2, v43
	s_waitcnt lgkmcnt(0)
	v_rcp_f32_e32 v54, v38
	v_lshl_add_u64 v[36:37], v[34:35], 0, s[0:1]
	v_bfe_u32 v38, v2, 16, 1
	s_movk_i32 s1, 0x7fff
	v_add3_u32 v2, v2, v38, s1
	v_add_co_u32_e32 v38, vcc, s80, v34
	v_rcp_f32_e32 v55, v39
	s_nop 0
	v_addc_co_u32_e32 v39, vcc, 0, v35, vcc
	global_store_short_d16_hi v[38:39], v2, off offset:768
	v_mul_f32_e32 v2, v18, v43
	v_bfe_u32 v18, v2, 16, 1
	v_add3_u32 v2, v2, v18, s1
	global_store_short_d16_hi v[36:37], v2, off offset:64
	v_mul_f32_e32 v2, v3, v44
	v_bfe_u32 v3, v2, 16, 1
	v_add3_u32 v2, v2, v3, s1
	global_store_short_d16_hi v[36:37], v2, off offset:2048
	v_mul_f32_e32 v2, v19, v44
	v_bfe_u32 v3, v2, 16, 1
	v_add3_u32 v2, v2, v3, s1
	global_store_short_d16_hi v[36:37], v2, off offset:2112
	v_mul_f32_e32 v2, v4, v45
	v_bfe_u32 v3, v2, 16, 1
	s_mov_b32 s0, 0x25bb1000
	v_add3_u32 v4, v2, v3, s1
	v_add_co_u32_e32 v2, vcc, s0, v34
	s_mov_b32 s0, 0x25bb4000
	s_nop 0
	v_addc_co_u32_e32 v3, vcc, 0, v35, vcc
	global_store_short_d16_hi v[2:3], v4, off offset:768
	v_mul_f32_e32 v4, v20, v45
	v_bfe_u32 v18, v4, 16, 1
	v_add3_u32 v4, v4, v18, s1
	global_store_short_d16_hi v[2:3], v4, off offset:832
	v_mul_f32_e32 v4, v5, v46
	v_bfe_u32 v5, v4, 16, 1
	v_add3_u32 v4, v4, v5, s1
	global_store_short_d16_hi v[2:3], v4, off offset:2816
	v_mul_f32_e32 v4, v21, v46
	v_bfe_u32 v5, v4, 16, 1
	v_add3_u32 v4, v4, v5, s1
	global_store_short_d16_hi v[2:3], v4, off offset:2880
	v_mul_f32_e32 v2, v6, v47
	v_bfe_u32 v3, v2, 16, 1
	v_add3_u32 v4, v2, v3, s1
	v_add_co_u32_e32 v2, vcc, s0, v34
	s_mov_b32 s0, 0x25bb5000
	s_nop 0
	v_addc_co_u32_e32 v3, vcc, 0, v35, vcc
	global_store_short_d16_hi v[2:3], v4, off offset:768
	v_mul_f32_e32 v4, v22, v47
	v_bfe_u32 v5, v4, 16, 1
	v_add3_u32 v4, v4, v5, s1
	global_store_short_d16_hi v[2:3], v4, off offset:832
	v_mul_f32_e32 v4, v7, v48
	v_bfe_u32 v5, v4, 16, 1
	v_add3_u32 v4, v4, v5, s1
	global_store_short_d16_hi v[2:3], v4, off offset:2816
	v_mul_f32_e32 v4, v23, v48
	v_bfe_u32 v5, v4, 16, 1
	v_add3_u32 v4, v4, v5, s1
	global_store_short_d16_hi v[2:3], v4, off offset:2880
	v_mul_f32_e32 v2, v8, v49
	v_bfe_u32 v3, v2, 16, 1
	v_add3_u32 v4, v2, v3, s1
	v_add_co_u32_e32 v2, vcc, s0, v34
	s_mov_b32 s0, 0x25bb8000
	s_nop 0
	v_addc_co_u32_e32 v3, vcc, 0, v35, vcc
	global_store_short_d16_hi v[2:3], v4, off offset:768
	v_mul_f32_e32 v4, v24, v49
	v_bfe_u32 v5, v4, 16, 1
	v_add3_u32 v4, v4, v5, s1
	global_store_short_d16_hi v[2:3], v4, off offset:832
	v_mul_f32_e32 v4, v9, v50
	v_bfe_u32 v5, v4, 16, 1
	v_add3_u32 v4, v4, v5, s1
	global_store_short_d16_hi v[2:3], v4, off offset:2816
	v_mul_f32_e32 v4, v25, v50
	v_bfe_u32 v5, v4, 16, 1
	v_add3_u32 v4, v4, v5, s1
	global_store_short_d16_hi v[2:3], v4, off offset:2880
	v_mul_f32_e32 v2, v10, v42
	v_bfe_u32 v3, v2, 16, 1
	v_add3_u32 v4, v2, v3, s1
	v_add_co_u32_e32 v2, vcc, s0, v34
	s_mov_b32 s0, 0x25bb9000
	s_nop 0
	v_addc_co_u32_e32 v3, vcc, 0, v35, vcc
	global_store_short_d16_hi v[2:3], v4, off offset:768
	v_mul_f32_e32 v4, v26, v42
	v_bfe_u32 v5, v4, 16, 1
	v_add3_u32 v4, v4, v5, s1
	global_store_short_d16_hi v[2:3], v4, off offset:832
	v_mul_f32_e32 v4, v11, v51
	v_bfe_u32 v5, v4, 16, 1
	v_add3_u32 v4, v4, v5, s1
	global_store_short_d16_hi v[2:3], v4, off offset:2816
	v_mul_f32_e32 v4, v27, v51
	v_bfe_u32 v5, v4, 16, 1
	v_add3_u32 v4, v4, v5, s1
	global_store_short_d16_hi v[2:3], v4, off offset:2880
	v_mul_f32_e32 v2, v12, v52
	v_bfe_u32 v3, v2, 16, 1
	v_add3_u32 v4, v2, v3, s1
	v_add_co_u32_e32 v2, vcc, s0, v34
	s_mov_b32 s0, 0x25bbc000
	s_nop 0
	v_addc_co_u32_e32 v3, vcc, 0, v35, vcc
	global_store_short_d16_hi v[2:3], v4, off offset:768
	v_mul_f32_e32 v4, v28, v52
	v_bfe_u32 v5, v4, 16, 1
	v_add3_u32 v4, v4, v5, s1
	global_store_short_d16_hi v[2:3], v4, off offset:832
	v_mul_f32_e32 v4, v13, v53
	v_bfe_u32 v5, v4, 16, 1
	v_add3_u32 v4, v4, v5, s1
	global_store_short_d16_hi v[2:3], v4, off offset:2816
	v_mul_f32_e32 v4, v29, v53
	v_bfe_u32 v5, v4, 16, 1
	v_add3_u32 v4, v4, v5, s1
	global_store_short_d16_hi v[2:3], v4, off offset:2880
	v_mul_f32_e32 v2, v14, v54
	v_bfe_u32 v3, v2, 16, 1
	v_add3_u32 v4, v2, v3, s1
	v_add_co_u32_e32 v2, vcc, s0, v34
	v_rcp_f32_e32 v40, v40
	s_nop 0
	v_addc_co_u32_e32 v3, vcc, 0, v35, vcc
	global_store_short_d16_hi v[2:3], v4, off offset:768
	v_mul_f32_e32 v4, v30, v54
	v_bfe_u32 v5, v4, 16, 1
	v_add3_u32 v4, v4, v5, s1
	global_store_short_d16_hi v[2:3], v4, off offset:832
	v_mul_f32_e32 v4, v15, v55
	v_bfe_u32 v5, v4, 16, 1
	v_add3_u32 v4, v4, v5, s1
	global_store_short_d16_hi v[2:3], v4, off offset:2816
	v_mul_f32_e32 v4, v31, v55
	v_bfe_u32 v5, v4, 16, 1
	v_add3_u32 v4, v4, v5, s1
	global_store_short_d16_hi v[2:3], v4, off offset:2880
	v_mul_f32_e32 v2, v16, v40
	v_bfe_u32 v3, v2, 16, 1
	s_mov_b32 s0, 0x25bbd000
	v_add3_u32 v4, v2, v3, s1
	v_add_co_u32_e32 v2, vcc, s0, v34
	v_rcp_f32_e32 v41, v41
	s_nop 0
	v_addc_co_u32_e32 v3, vcc, 0, v35, vcc
	global_store_short_d16_hi v[2:3], v4, off offset:768
	v_mul_f32_e32 v4, v32, v40
	v_bfe_u32 v5, v4, 16, 1
	v_add3_u32 v4, v4, v5, s1
	global_store_short_d16_hi v[2:3], v4, off offset:832
	v_mul_f32_e32 v4, v17, v41
	v_bfe_u32 v5, v4, 16, 1
	v_add3_u32 v4, v4, v5, s1
	global_store_short_d16_hi v[2:3], v4, off offset:2816
	v_mul_f32_e32 v4, v33, v41
	v_bfe_u32 v5, v4, 16, 1
	v_add3_u32 v4, v4, v5, s1
	global_store_short_d16_hi v[2:3], v4, off offset:2880
	v_mov_b32_e32 v2, v0
	s_barrier
	s_barrier
	s_nop 0
	v_cmp_eq_u32_e32 vcc, 0, v2
	s_and_saveexec_b64 s[0:1], vcc
	s_cbranch_execz .LBB0_1415
	v_readlane_b32 s4, v252, 14
	s_mov_b64 s[2:3], exec
	s_nop 0
	v_mov_b32_e32 v2, s4
	ds_write_b32 v2, v154
	v_mbcnt_lo_u32_b32 v2, s2, 0
	v_mbcnt_hi_u32_b32 v2, s3, v2
	v_cmp_eq_u32_e32 vcc, 0, v2
	s_and_saveexec_b64 s[4:5], vcc
	s_cbranch_execz .LBB0_1414
	s_bcnt1_i32_b64 s2, s[2:3]
	v_mov_b32_e32 v3, s2
	v_readlane_b32 s2, v253, 19
	v_readlane_b32 s3, v253, 20
	s_nop 4
	global_atomic_add v3, v83, v3, s[2:3] sc0
	s_branch .LBB0_1414
